# MoBA/FoX: ten of the sixteen V fragment reads hoisted into the H1 tail; early P.V MFMAs start on the o[1] half
# baseline (speedup 1.0000x reference)
; __device__ __forceinline__ unsigned cvtpk(float lo, float hi) { f32x2_t v = {lo, hi}; bf16x2_t b = __builtin_convertvector(v, bf16x2_t); return __builtin_bit_cast(unsigned, b); }
; __device__ __forceinline__ s16x4 vtr(lds_cptr p) { return __builtin_bit_cast(s16x4, __builtin_amdgcn_ds_read_tr16_b64_v4i16((__attribute__((address_space(3))) v4i16_t*)p)); }
; template <class BIAS>
; __device__ __forceinline__ void attn_tiles(char* shm, const UnitIO& io, int t_begin, int t_end, const BIAS& B, int tid) {
;     ...
;             for (int d0 = 0; d0 < 4; ++d0) { c0 = __builtin_amdgcn_mfma_f32_32x32x16_bf16(kf[2 * d0], qr[d0], c0, 0, 0, 0); c1 = __builtin_amdgcn_mfma_f32_32x32x16_bf16(kf[2 * d0 + 1], qr[d0], c1, 0, 0, 0); }
;             float s0 = 0.f;
; #pragma unroll
;             for (int r = 0; r < 16; ++r) c0[r] = __builtin_amdgcn_exp2f(c0[r]);
;             { f32x2_t s2 = (f32x2_t){c0[0], c0[1]};
; #pragma unroll
;               for (int i = 1; i < 8; ++i) s2 += (f32x2_t){c0[2 * i], c0[2 * i + 1]};
;               s0 = s2[0] + s2[1]; }
;             l_reg += s0;
; #pragma unroll
;             for (int i = 0; i < 4; ++i) { pw[0][i] = cvtpk(c0[2 * i], c0[2 * i + 1]); pw[1][i] = cvtpk(c0[8 + 2 * i], c0[9 + 2 * i]); }
;             c1x = c1;
;         }
;         if (act) {
;             const lds_cptr vp = vp0 + sl_c;
;             s16x4 vlo[8], vhi[8];
; #pragma unroll
;             for (int i = 0; i < 8; ++i) { vlo[i] = vtr(vp + (i >> 2) * 4096 + (i & 3) * 1024); vhi[i] = vtr(vp + (i >> 2) * 4096 + (i & 3) * 1024 + 512); }
.Lmo_go:
	v_exp_f32_e32 v50, v50
	v_exp_f32_e32 v51, v51
	v_exp_f32_e32 v52, v52
	v_exp_f32_e32 v53, v53
	v_mfma_f32_32x32x16_bf16 v[34:49], v[90:93], v[70:73], v[34:49]
	v_exp_f32_e32 v98, v54
	v_exp_f32_e32 v99, v55
	v_exp_f32_e32 v100, v56
	v_exp_f32_e32 v101, v57
	v_mfma_f32_32x32x16_bf16 v[34:49], v[86:89], v[74:77], v[34:49]
	v_exp_f32_e32 v54, v58
	v_exp_f32_e32 v55, v59
	v_exp_f32_e32 v56, v60
	v_exp_f32_e32 v57, v61
	v_mfma_f32_32x32x16_bf16 v[34:49], v[82:85], v[78:81], v[34:49]
	v_add_u32_e32 v104, s23, v180
	ds_read_b64_tr_b16 v[82:83], v104 offset:34816
	ds_read_b64_tr_b16 v[84:85], v104 offset:35328
	ds_read_b64_tr_b16 v[86:87], v104 offset:35840
	ds_read_b64_tr_b16 v[88:89], v104 offset:36352
	ds_read_b64_tr_b16 v[90:91], v104 offset:36864
	ds_read_b64_tr_b16 v[92:93], v104 offset:37376
	ds_read_b64_tr_b16 v[94:95], v104 offset:37888
	ds_read_b64_tr_b16 v[96:97], v104 offset:38400
	ds_read_b64_tr_b16 v[102:103], v104 offset:39936
	ds_read_b64_tr_b16 v[104:105], v104 offset:40448
	v_exp_f32_e32 v58, v62
	v_exp_f32_e32 v59, v63
	v_add_f32_e32 v62, v50, v52
	v_add_f32_e32 v63, v51, v53
	v_add_f32_e64 v62, v98, v62
	v_add_f32_e64 v63, v99, v63
	v_exp_f32_e32 v60, v64
	v_exp_f32_e32 v61, v65
	v_add_f32_e32 v62, v100, v62
	v_add_f32_e32 v63, v101, v63
	v_cvt_pk_bf16_f32 v50, v50, v51
	v_add_f32_e32 v62, v54, v62
	v_add_f32_e32 v63, v55, v63
	v_cvt_pk_bf16_f32 v54, v54, v55
	v_add_f32_e32 v62, v56, v62
	v_add_f32_e32 v63, v57, v63
	v_cvt_pk_bf16_f32 v51, v52, v53
	v_add_f32_e32 v62, v58, v62
	v_add_f32_e32 v63, v59, v63
	v_cvt_pk_bf16_f32 v55, v56, v57
	v_add_f32_e32 v62, v60, v62
	v_add_f32_e32 v63, v61, v63
	v_cvt_pk_bf16_f32 v52, v98, v99
	v_add_f32_e32 v62, v62, v63
	v_cvt_pk_bf16_f32 v56, v58, v59
	v_cvt_pk_bf16_f32 v53, v100, v101
	v_cvt_pk_bf16_f32 v57, v60, v61
	v_add_f32_e32 v139, v139, v62
	s_and_b64 vcc, exec, s[4:5]
	s_cbranch_vccz .LBB0_311

; __device__ __forceinline__ unsigned cvtpk(float lo, float hi) { f32x2_t v = {lo, hi}; bf16x2_t b = __builtin_convertvector(v, bf16x2_t); return __builtin_bit_cast(unsigned, b); }
; __device__ __forceinline__ s16x4 vtr(lds_cptr p) { return __builtin_bit_cast(s16x4, __builtin_amdgcn_ds_read_tr16_b64_v4i16((__attribute__((address_space(3))) v4i16_t*)p)); }
; #define ATT_SBAR() __builtin_amdgcn_sched_barrier(0)
; template <class BIAS>
; __device__ __forceinline__ void attn_tiles(char* shm, const UnitIO& io, int t_begin, int t_end, const BIAS& B, int tid) {
;     ...
;         if (act) {
;             const lds_cptr vp = vp0 + sl_c;
;             s16x4 vlo[8], vhi[8];
; #pragma unroll
;             for (int i = 0; i < 8; ++i) { vlo[i] = vtr(vp + (i >> 2) * 4096 + (i & 3) * 1024); vhi[i] = vtr(vp + (i >> 2) * 4096 + (i & 3) * 1024 + 512); }
;             ATT_SBAR();
;             { float s1 = 0.f;
; #pragma unroll
;               for (int r = 0; r < 16; ++r) c1x[r] = __builtin_amdgcn_exp2f(c1x[r]);
;               { f32x2_t s2 = (f32x2_t){c1x[0], c1x[1]};
; #pragma unroll
;                 for (int i = 1; i < 8; ++i) s2 += (f32x2_t){c1x[2 * i], c1x[2 * i + 1]};
;                 s1 = s2[0] + s2[1]; }
;               l_reg += s1;
; #pragma unroll
;               for (int i = 0; i < 4; ++i) { pw[2][i] = cvtpk(c1x[2 * i], c1x[2 * i + 1]); pw[3][i] = cvtpk(c1x[8 + 2 * i], c1x[9 + 2 * i]); } }
;             ATT_SBAR();
;             asm volatile("" : "+v"(vlo[0]), "+v"(vhi[0]), "+v"(vlo[1]), "+v"(vhi[1]), "+v"(vlo[2]), "+v"(vhi[2]), "+v"(vlo[3]), "+v"(vhi[3]));
; #pragma unroll
;             for (int ks = 0; ks < 4; ++ks) { const bf16x8 vf = (bf16x8){vlo[ks][0], vlo[ks][1], vlo[ks][2], vlo[ks][3], vhi[ks][0], vhi[ks][1], vhi[ks][2], vhi[ks][3]};
;                 o[0] = __builtin_amdgcn_mfma_f32_32x32x16_bf16(__builtin_bit_cast(bf16x8, pw[ks]), vf, o[0], 0, 0, 0); }
;             ATT_SBAR();
;             asm volatile("" : "+v"(vlo[4]), "+v"(vhi[4]), "+v"(vlo[5]), "+v"(vhi[5]), "+v"(vlo[6]), "+v"(vhi[6]), "+v"(vlo[7]), "+v"(vhi[7]));
; #pragma unroll
;             for (int ks = 0; ks < 4; ++ks) { const bf16x8 vf = (bf16x8){vlo[4 + ks][0], vlo[4 + ks][1], vlo[4 + ks][2], vlo[4 + ks][3], vhi[4 + ks][0], vhi[4 + ks][1], vhi[4 + ks][2], vhi[4 + ks][3]};
;                 o[1] = __builtin_amdgcn_mfma_f32_32x32x16_bf16(__builtin_bit_cast(bf16x8, pw[ks]), vf, o[1], 0, 0, 0); }
.LBB0_311:
	v_add_u32_e32 v106, s23, v180
	ds_read_b64_tr_b16 v[58:59], v106 offset:32768
	ds_read_b64_tr_b16 v[60:61], v106 offset:33280
	ds_read_b64_tr_b16 v[62:63], v106 offset:33792
	ds_read_b64_tr_b16 v[64:65], v106 offset:34304
	ds_read_b64_tr_b16 v[98:99], v106 offset:38912
	ds_read_b64_tr_b16 v[100:101], v106 offset:39424
	v_exp_f32_e32 v34, v34
	v_exp_f32_e32 v35, v35
	v_exp_f32_e32 v36, v36
	v_exp_f32_e32 v37, v37
	s_waitcnt lgkmcnt(10)
	v_mfma_f32_32x32x16_bf16 v[18:33], v[50:53], v[90:93], v[18:33]
	v_exp_f32_e32 v38, v38
	v_exp_f32_e32 v39, v39
	v_exp_f32_e32 v40, v40
	v_exp_f32_e32 v41, v41
	s_waitcnt lgkmcnt(8)
	v_mfma_f32_32x32x16_bf16 v[18:33], v[54:57], v[94:97], v[18:33]
	v_exp_f32_e32 v42, v42
	v_exp_f32_e32 v43, v43
	v_exp_f32_e32 v44, v44
	v_exp_f32_e32 v45, v45
	s_waitcnt lgkmcnt(4)
	v_mfma_f32_32x32x16_bf16 v[2:17], v[50:53], v[58:61], v[2:17]
	v_add_f32_e32 v106, v36, v34
	v_add_f32_e32 v107, v37, v35
	v_exp_f32_e32 v46, v46
	v_exp_f32_e32 v47, v47
	s_waitcnt lgkmcnt(2)
	v_mfma_f32_32x32x16_bf16 v[2:17], v[54:57], v[62:65], v[2:17]
	v_add_f32_e32 v106, v38, v106
	v_add_f32_e32 v107, v39, v107
	v_exp_f32_e32 v48, v48
	v_exp_f32_e32 v49, v49
	v_add_f32_e32 v106, v40, v106
	v_add_f32_e32 v107, v41, v107
	v_cvt_pk_bf16_f32 v110, v42, v43
	v_add_f32_e32 v106, v42, v106
	v_add_f32_e32 v107, v43, v107
	v_cvt_pk_bf16_f32 v111, v44, v45
	v_add_f32_e32 v106, v44, v106
	v_add_f32_e32 v107, v45, v107
	v_cvt_pk_bf16_f32 v108, v38, v39
	v_add_f32_e32 v106, v46, v106
	v_add_f32_e32 v107, v47, v107
	v_cvt_pk_bf16_f32 v112, v46, v47
	v_add_f32_e32 v106, v48, v106
	v_add_f32_e32 v107, v49, v107
	v_cvt_pk_bf16_f32 v109, v40, v41
	v_add_f32_e32 v117, v106, v107
	v_cvt_pk_bf16_f32 v106, v34, v35
	v_cvt_pk_bf16_f32 v107, v36, v37
	v_cvt_pk_bf16_f32 v113, v48, v49
	s_waitcnt lgkmcnt(0)
	s_nop 0
	v_mfma_f32_32x32x16_bf16 v[2:17], v[106:109], v[82:85], v[2:17]
	v_mfma_f32_32x32x16_bf16 v[2:17], v[110:113], v[86:89], v[2:17]
	v_add_f32_e32 v139, v139, v117
	v_mfma_f32_32x32x16_bf16 v[18:33], v[106:109], v[98:101], v[18:33]
	v_mfma_f32_32x32x16_bf16 v[18:33], v[110:113], v[102:105], v[18:33]
	s_mov_b64 s[4:5], -1
	s_and_b64 vcc, exec, s[12:13]
	s_cbranch_vccnz .LBB0_305

; __device__ __forceinline__ unsigned cvtpk(float lo, float hi) { f32x2_t v = {lo, hi}; bf16x2_t b = __builtin_convertvector(v, bf16x2_t); return __builtin_bit_cast(unsigned, b); }
; __device__ __forceinline__ s16x4 vtr(lds_cptr p) { return __builtin_bit_cast(s16x4, __builtin_amdgcn_ds_read_tr16_b64_v4i16((__attribute__((address_space(3))) v4i16_t*)p)); }
; template <class BIAS>
; __device__ __forceinline__ void attn_tiles(char* shm, const UnitIO& io, int t_begin, int t_end, const BIAS& B, int tid) {
;     ...
;             for (int d0 = 0; d0 < 4; ++d0) { c0 = __builtin_amdgcn_mfma_f32_32x32x16_bf16(kf[2 * d0], qr[d0], c0, 0, 0, 0); c1 = __builtin_amdgcn_mfma_f32_32x32x16_bf16(kf[2 * d0 + 1], qr[d0], c1, 0, 0, 0); }
;             float s0 = 0.f;
; #pragma unroll
;             for (int r = 0; r < 16; ++r) c0[r] = __builtin_amdgcn_exp2f(c0[r]);
;             { f32x2_t s2 = (f32x2_t){c0[0], c0[1]};
; #pragma unroll
;               for (int i = 1; i < 8; ++i) s2 += (f32x2_t){c0[2 * i], c0[2 * i + 1]};
;               s0 = s2[0] + s2[1]; }
;             l_reg += s0;
; #pragma unroll
;             for (int i = 0; i < 4; ++i) { pw[0][i] = cvtpk(c0[2 * i], c0[2 * i + 1]); pw[1][i] = cvtpk(c0[8 + 2 * i], c0[9 + 2 * i]); }
;             c1x = c1;
;         }
;         if (act) {
;             const lds_cptr vp = vp0 + sl_c;
;             s16x4 vlo[8], vhi[8];
; #pragma unroll
;             for (int i = 0; i < 8; ++i) { vlo[i] = vtr(vp + (i >> 2) * 4096 + (i & 3) * 1024); vhi[i] = vtr(vp + (i >> 2) * 4096 + (i & 3) * 1024 + 512); }
.Lfx_go:
	v_exp_f32_e32 v66, v66
	v_exp_f32_e32 v67, v67
	v_exp_f32_e32 v68, v68
	v_exp_f32_e32 v69, v69
	v_mfma_f32_32x32x16_bf16 v[50:65], v[106:109], v[86:89], v[50:65]
	v_exp_f32_e32 v114, v70
	v_exp_f32_e32 v115, v71
	v_exp_f32_e32 v116, v72
	v_exp_f32_e32 v117, v73
	v_mfma_f32_32x32x16_bf16 v[50:65], v[102:105], v[90:93], v[50:65]
	v_exp_f32_e32 v70, v74
	v_exp_f32_e32 v71, v75
	v_exp_f32_e32 v72, v76
	v_exp_f32_e32 v73, v77
	v_mfma_f32_32x32x16_bf16 v[50:65], v[98:101], v[94:97], v[50:65]
	v_add_u32_e32 v120, s20, v180
	ds_read_b64_tr_b16 v[98:99], v120 offset:34816
	ds_read_b64_tr_b16 v[100:101], v120 offset:35328
	ds_read_b64_tr_b16 v[102:103], v120 offset:35840
	ds_read_b64_tr_b16 v[104:105], v120 offset:36352
	ds_read_b64_tr_b16 v[106:107], v120 offset:36864
	ds_read_b64_tr_b16 v[108:109], v120 offset:37376
	ds_read_b64_tr_b16 v[110:111], v120 offset:37888
	ds_read_b64_tr_b16 v[112:113], v120 offset:38400
	ds_read_b64_tr_b16 v[118:119], v120 offset:39936
	ds_read_b64_tr_b16 v[120:121], v120 offset:40448
	v_exp_f32_e32 v74, v78
	v_exp_f32_e32 v75, v79
	v_add_f32_e32 v78, v66, v68
	v_add_f32_e32 v79, v67, v69
	v_add_f32_e64 v78, v114, v78
	v_add_f32_e64 v79, v115, v79
	v_exp_f32_e32 v76, v80
	v_exp_f32_e32 v77, v81
	v_add_f32_e32 v78, v116, v78
	v_add_f32_e32 v79, v117, v79
	v_cvt_pk_bf16_f32 v66, v66, v67
	v_add_f32_e32 v78, v70, v78
	v_add_f32_e32 v79, v71, v79
	v_cvt_pk_bf16_f32 v70, v70, v71
	v_add_f32_e32 v78, v72, v78
	v_add_f32_e32 v79, v73, v79
	v_cvt_pk_bf16_f32 v67, v68, v69
	v_add_f32_e32 v78, v74, v78
	v_add_f32_e32 v79, v75, v79
	v_cvt_pk_bf16_f32 v71, v72, v73
	v_add_f32_e32 v78, v76, v78
	v_add_f32_e32 v79, v77, v79
	v_cvt_pk_bf16_f32 v68, v114, v115
	v_add_f32_e32 v78, v78, v79
	v_cvt_pk_bf16_f32 v72, v74, v75
	v_cvt_pk_bf16_f32 v69, v116, v117
	v_cvt_pk_bf16_f32 v73, v76, v77
	v_add_f32_e32 v135, v135, v78
	s_and_b64 vcc, exec, s[34:35]
	s_cbranch_vccz .LBB0_355

; __device__ __forceinline__ unsigned cvtpk(float lo, float hi) { f32x2_t v = {lo, hi}; bf16x2_t b = __builtin_convertvector(v, bf16x2_t); return __builtin_bit_cast(unsigned, b); }
; __device__ __forceinline__ s16x4 vtr(lds_cptr p) { return __builtin_bit_cast(s16x4, __builtin_amdgcn_ds_read_tr16_b64_v4i16((__attribute__((address_space(3))) v4i16_t*)p)); }
; #define ATT_SBAR() __builtin_amdgcn_sched_barrier(0)
; template <class BIAS>
; __device__ __forceinline__ void attn_tiles(char* shm, const UnitIO& io, int t_begin, int t_end, const BIAS& B, int tid) {
;     ...
;         if (act) {
;             const lds_cptr vp = vp0 + sl_c;
;             s16x4 vlo[8], vhi[8];
; #pragma unroll
;             for (int i = 0; i < 8; ++i) { vlo[i] = vtr(vp + (i >> 2) * 4096 + (i & 3) * 1024); vhi[i] = vtr(vp + (i >> 2) * 4096 + (i & 3) * 1024 + 512); }
;             ATT_SBAR();
;             { float s1 = 0.f;
; #pragma unroll
;               for (int r = 0; r < 16; ++r) c1x[r] = __builtin_amdgcn_exp2f(c1x[r]);
;               { f32x2_t s2 = (f32x2_t){c1x[0], c1x[1]};
; #pragma unroll
;                 for (int i = 1; i < 8; ++i) s2 += (f32x2_t){c1x[2 * i], c1x[2 * i + 1]};
;                 s1 = s2[0] + s2[1]; }
;               l_reg += s1;
; #pragma unroll
;               for (int i = 0; i < 4; ++i) { pw[2][i] = cvtpk(c1x[2 * i], c1x[2 * i + 1]); pw[3][i] = cvtpk(c1x[8 + 2 * i], c1x[9 + 2 * i]); } }
;             ATT_SBAR();
;             asm volatile("" : "+v"(vlo[0]), "+v"(vhi[0]), "+v"(vlo[1]), "+v"(vhi[1]), "+v"(vlo[2]), "+v"(vhi[2]), "+v"(vlo[3]), "+v"(vhi[3]));
; #pragma unroll
;             for (int ks = 0; ks < 4; ++ks) { const bf16x8 vf = (bf16x8){vlo[ks][0], vlo[ks][1], vlo[ks][2], vlo[ks][3], vhi[ks][0], vhi[ks][1], vhi[ks][2], vhi[ks][3]};
;                 o[0] = __builtin_amdgcn_mfma_f32_32x32x16_bf16(__builtin_bit_cast(bf16x8, pw[ks]), vf, o[0], 0, 0, 0); }
;             ATT_SBAR();
;             asm volatile("" : "+v"(vlo[4]), "+v"(vhi[4]), "+v"(vlo[5]), "+v"(vhi[5]), "+v"(vlo[6]), "+v"(vhi[6]), "+v"(vlo[7]), "+v"(vhi[7]));
; #pragma unroll
;             for (int ks = 0; ks < 4; ++ks) { const bf16x8 vf = (bf16x8){vlo[4 + ks][0], vlo[4 + ks][1], vlo[4 + ks][2], vlo[4 + ks][3], vhi[4 + ks][0], vhi[4 + ks][1], vhi[4 + ks][2], vhi[4 + ks][3]};
;                 o[1] = __builtin_amdgcn_mfma_f32_32x32x16_bf16(__builtin_bit_cast(bf16x8, pw[ks]), vf, o[1], 0, 0, 0); }
.LBB0_355:
	v_add_u32_e32 v122, s20, v180
	ds_read_b64_tr_b16 v[74:75], v122 offset:32768
	ds_read_b64_tr_b16 v[76:77], v122 offset:33280
	ds_read_b64_tr_b16 v[78:79], v122 offset:33792
	ds_read_b64_tr_b16 v[80:81], v122 offset:34304
	ds_read_b64_tr_b16 v[114:115], v122 offset:38912
	ds_read_b64_tr_b16 v[116:117], v122 offset:39424
	v_exp_f32_e32 v50, v50
	v_exp_f32_e32 v51, v51
	v_exp_f32_e32 v52, v52
	v_exp_f32_e32 v53, v53
	s_waitcnt lgkmcnt(10)
	v_mfma_f32_32x32x16_bf16 v[34:49], v[66:69], v[106:109], v[34:49]
	v_exp_f32_e32 v54, v54
	v_exp_f32_e32 v55, v55
	v_exp_f32_e32 v56, v56
	v_exp_f32_e32 v57, v57
	s_waitcnt lgkmcnt(8)
	v_mfma_f32_32x32x16_bf16 v[34:49], v[70:73], v[110:113], v[34:49]
	v_exp_f32_e32 v58, v58
	v_exp_f32_e32 v59, v59
	v_exp_f32_e32 v60, v60
	v_exp_f32_e32 v61, v61
	s_waitcnt lgkmcnt(4)
	v_mfma_f32_32x32x16_bf16 v[12:27], v[66:69], v[74:77], v[12:27]
	v_add_f32_e32 v122, v52, v50
	v_add_f32_e32 v123, v53, v51
	v_exp_f32_e32 v62, v62
	v_exp_f32_e32 v63, v63
	s_waitcnt lgkmcnt(2)
	v_mfma_f32_32x32x16_bf16 v[12:27], v[70:73], v[78:81], v[12:27]
	v_add_f32_e32 v122, v54, v122
	v_add_f32_e32 v123, v55, v123
	v_exp_f32_e32 v64, v64
	v_exp_f32_e32 v65, v65
	v_add_f32_e32 v122, v56, v122
	v_add_f32_e32 v123, v57, v123
	v_cvt_pk_bf16_f32 v126, v58, v59
	v_add_f32_e32 v122, v58, v122
	v_add_f32_e32 v123, v59, v123
	v_cvt_pk_bf16_f32 v127, v60, v61
	v_add_f32_e32 v122, v60, v122
	v_add_f32_e32 v123, v61, v123
	v_cvt_pk_bf16_f32 v124, v54, v55
	v_add_f32_e32 v122, v62, v122
	v_add_f32_e32 v123, v63, v123
	v_cvt_pk_bf16_f32 v128, v62, v63
	v_add_f32_e32 v122, v64, v122
	v_add_f32_e32 v123, v65, v123
	v_cvt_pk_bf16_f32 v125, v56, v57
	v_add_f32_e32 v139, v122, v123
	v_cvt_pk_bf16_f32 v122, v50, v51
	v_cvt_pk_bf16_f32 v123, v52, v53
	v_cvt_pk_bf16_f32 v129, v64, v65
	s_waitcnt lgkmcnt(0)
	s_nop 0
	v_mfma_f32_32x32x16_bf16 v[12:27], v[122:125], v[98:101], v[12:27]
	v_mfma_f32_32x32x16_bf16 v[12:27], v[126:129], v[102:105], v[12:27]
	v_add_f32_e32 v135, v135, v139
	v_mfma_f32_32x32x16_bf16 v[34:49], v[122:125], v[114:117], v[34:49]
	v_mfma_f32_32x32x16_bf16 v[34:49], v[126:129], v[118:121], v[34:49]
	s_mov_b64 s[34:35], -1
	s_and_b64 vcc, exec, s[46:47]
	s_cbranch_vccnz .LBB0_349
